# baseline (speedup 1.0000x reference)
_Z11gemm_kernelPKfPKDF16bS0_Pf:
	s_and_b32 s3, s2, 7
	s_ashr_i32 s14, s2, 3
	s_lshl_b32 s12, s3, 6
	s_load_dwordx8 s[4:11], s[0:1], 0x0
	s_add_i32 s12, s12, s14
	s_bfe_u32 s18, s2, 0x10002
	s_lshl_b32 s2, s12, 6
	s_lshl_b32 s13, s18, 14
	s_and_b32 s2, s2, 0x3f00
	v_lshrrev_b32_e32 v52, 6, v0
	v_and_b32_e32 v50, 15, v0
	v_bfe_u32 v51, v0, 4, 2
	v_bfe_u32 v1, v0, 3, 3
	s_or_b32 s2, s2, s13
	v_lshl_or_b32 v102, v52, 2, v51
	v_lshl_or_b32 v104, v52, 3, v1
	v_lshlrev_b32_e32 v1, 4, v50
	s_lshl_b32 s15, s2, 9
	s_waitcnt lgkmcnt(0)
	v_readfirstlane_b32 s26, v0
	v_and_b32_e32 v238, 3, v52
	v_lshlrev_b32_e32 v238, 6, v238
	v_lshl_or_b32 v238, v51, 2, v238
	v_lshlrev_b32_e32 v238, 2, v238
	s_and_b32 s24, s12, 3
	s_lshl_b32 s24, s24, 8
	s_lshl_b32 s25, s18, 10
	s_add_u32 s24, s24, s25
	s_lshl_b32 s24, s24, 2
	s_add_u32 s24, s8, s24
	s_addc_u32 s25, s9, 0
	s_lshr_b32 s26, s26, 8
	global_load_dwordx4 v[240:243], v238, s[24:25]
	global_load_dwordx4 v[244:247], v238, s[24:25] offset:64
	global_load_dwordx4 v[248:251], v238, s[24:25] offset:128
	global_load_dwordx4 v[252:255], v238, s[24:25] offset:192
	s_mov_b64 s[0:1], s[6:7]
	s_and_b32 s5, s5, 0xffff
	s_mov_b32 s7, 0x20000
	s_brev_b32 s6, -2
	v_lshl_or_b32 v1, v102, 9, v1
	s_or_b32 s2, s15, 0x4000
	s_lshl_b32 s14, s14, 8
	v_lshlrev_b32_e32 v103, 3, v0
	buffer_load_dwordx4 v[54:57], v1, s[4:7], s15 offen sc0 nt
	buffer_load_dwordx4 v[58:61], v1, s[4:7], s2 offen sc0 nt
	s_or_b32 s2, s15, 0x8000
	s_or_b32 s3, s15, 0xc000
	s_lshl_b32 s19, s18, 10
	s_and_b32 s20, s14, 0x300
	v_and_b32_e32 v105, 56, v103
	buffer_load_dwordx4 v[62:65], v1, s[4:7], s2 offen sc0 nt
	buffer_load_dwordx4 v[66:69], v1, s[4:7], s3 offen sc0 nt
	s_or_b32 s2, s15, 0x10000
	s_or_b32 s3, s15, 0x14000
	s_or_b32 s14, s19, s20
	v_lshlrev_b32_e32 v106, 1, v105
	buffer_load_dwordx4 v[70:73], v1, s[4:7], s2 offen sc0 nt
	buffer_load_dwordx4 v[74:77], v1, s[4:7], s3 offen sc0 nt
	s_or_b32 s2, s15, 0x18000
	s_or_b32 s3, s15, 0x1c000
	s_lshl_b32 s14, s14, 11
	buffer_load_dwordx4 v[78:81], v1, s[4:7], s2 offen sc0 nt
	buffer_load_dwordx4 v[82:85], v1, s[4:7], s3 offen sc0 nt
	s_and_b32 s1, s1, 0xffff
	s_mov_b32 s2, s6
	s_mov_b32 s3, s7
	v_lshl_or_b32 v188, v104, 11, v106
	s_or_b32 s16, s14, 0x20000
	buffer_load_dwordx4 v[86:89], v188, s[0:3], s14 offen sc1
	buffer_load_dwordx4 v[90:93], v188, s[0:3], s16 offen sc1
	s_or_b32 s16, s14, 0x40000
	s_or_b32 s17, s14, 0x60000
	buffer_load_dwordx4 v[94:97], v188, s[0:3], s16 offen sc1
	buffer_load_dwordx4 v[98:101], v188, s[0:3], s17 offen sc1
	s_or_b32 s16, s15, 0x100
	s_or_b32 s17, s15, 0x4100
	buffer_load_dwordx4 v[10:13], v1, s[4:7], s16 offen sc0 nt
	buffer_load_dwordx4 v[18:21], v1, s[4:7], s17 offen sc0 nt
	s_or_b32 s16, s15, 0x8100
	s_or_b32 s17, s15, 0xc100
	buffer_load_dwordx4 v[22:25], v1, s[4:7], s16 offen sc0 nt
	buffer_load_dwordx4 v[30:33], v1, s[4:7], s17 offen sc0 nt
	s_or_b32 s16, s15, 0x10100
	s_or_b32 s17, s15, 0x14100
	buffer_load_dwordx4 v[34:37], v1, s[4:7], s16 offen sc0 nt
	buffer_load_dwordx4 v[38:41], v1, s[4:7], s17 offen sc0 nt
	s_or_b32 s16, s15, 0x18100
	s_or_b32 s15, s15, 0x1c100
	buffer_load_dwordx4 v[42:45], v1, s[4:7], s16 offen sc0 nt
	buffer_load_dwordx4 v[46:49], v1, s[4:7], s15 offen sc0 nt
	s_or_b32 s15, s14, 0x80
	s_or_b32 s16, s14, 0x20080
	buffer_load_dwordx4 v[2:5], v188, s[0:3], s15 offen sc1
	buffer_load_dwordx4 v[6:9], v188, s[0:3], s16 offen sc1
	s_or_b32 s15, s14, 0x40080
	s_or_b32 s16, s14, 0x60080
	buffer_load_dwordx4 v[14:17], v188, s[0:3], s15 offen sc1
	buffer_load_dwordx4 v[26:29], v188, s[0:3], s16 offen sc1
	v_lshrrev_b32_e32 v107, 7, v0
	v_bfe_u32 v108, v0, 3, 1
	v_lshlrev_b32_e32 v102, 6, v102
	s_movk_i32 s2, 0x3c0
	v_and_or_b32 v102, v102, s2, v105
	v_lshrrev_b32_e32 v105, 2, v0
	v_and_or_b32 v107, v107, 2, v108
	v_and_b32_e32 v105, 32, v105
	v_lshlrev_b32_e32 v107, 10, v107
	v_bfe_u32 v103, v103, 5, 1
	v_lshlrev_b32_e32 v104, 6, v104
	v_and_b32_e32 v106, 48, v106
	v_bitop3_b32 v189, v102, v107, v105 bitop3:0xde
	v_and_or_b32 v103, v52, 6, v103
	v_and_or_b32 v104, v104, s2, v106
	v_lshrrev_b32_e32 v106, 1, v0
	v_lshlrev_b32_e32 v103, 10, v103
	v_and_b32_e32 v106, 32, v106
	v_bitop3_b32 v190, v104, v103, v106 bitop3:0xde
	v_lshrrev_b32_e32 v53, 8, v0
	s_movk_i32 s15, 0x4000
	s_mov_b32 s16, 0x8000
	s_mov_b32 s17, 0xc000
	s_waitcnt vmcnt(23)
	v_cvt_pk_bf16_f32 v57, v56, v57
	v_cvt_pk_bf16_f32 v56, v54, v55
	s_waitcnt vmcnt(22)
	v_cvt_pk_bf16_f32 v55, v60, v61
	v_cvt_pk_bf16_f32 v54, v58, v59
	ds_write2st64_b64 v189, v[56:57], v[54:55] offset1:8
	s_waitcnt vmcnt(21)
	v_cvt_pk_bf16_f32 v55, v64, v65
	v_cvt_pk_bf16_f32 v54, v62, v63
	s_waitcnt vmcnt(20)
	v_cvt_pk_bf16_f32 v57, v68, v69
	v_cvt_pk_bf16_f32 v56, v66, v67
	ds_write2st64_b64 v189, v[54:55], v[56:57] offset0:16 offset1:24
	s_waitcnt vmcnt(19)
	v_cvt_pk_bf16_f32 v55, v72, v73
	v_cvt_pk_bf16_f32 v54, v70, v71
	s_waitcnt vmcnt(18)
	v_cvt_pk_bf16_f32 v57, v76, v77
	v_cvt_pk_bf16_f32 v56, v74, v75
	ds_write2st64_b64 v189, v[54:55], v[56:57] offset0:32 offset1:40
	s_waitcnt vmcnt(17)
	v_cvt_pk_bf16_f32 v55, v80, v81
	v_cvt_pk_bf16_f32 v54, v78, v79
	s_waitcnt vmcnt(16)
	v_cvt_pk_bf16_f32 v57, v84, v85
	v_cvt_pk_bf16_f32 v56, v82, v83
	ds_write2st64_b64 v189, v[54:55], v[56:57] offset0:48 offset1:56
	s_waitcnt vmcnt(15)
	ds_write_b128 v190, v[86:89] offset:32768
	s_waitcnt vmcnt(14)
	ds_write_b128 v190, v[90:93] offset:40960
	s_waitcnt vmcnt(13)
	ds_write_b128 v190, v[94:97] offset:49152
	s_waitcnt vmcnt(12)
	ds_write_b128 v190, v[98:101] offset:57344
	s_waitcnt lgkmcnt(0)
	s_barrier
	v_cmp_eq_u32_e32 vcc, 1, v53
	s_and_saveexec_b64 s[2:3], vcc
	s_cbranch_execz .LBB1_2
	s_barrier

.LBB1_4:
	v_add_u32_e32 v182, s19, v191
	v_add_u32_e32 v238, s19, v192
	ds_read_b128 v[178:181], v182 offset:32768
	ds_read_b128 v[194:197], v182 offset:34816
	ds_read_b128 v[198:201], v182 offset:36864
	ds_read_b128 v[202:205], v182 offset:38912
	ds_read_b128 v[206:209], v238
	ds_read_b128 v[210:213], v238 offset:2048
	ds_read_b128 v[214:217], v238 offset:4096
	ds_read_b128 v[218:221], v238 offset:6144
	ds_read_b128 v[222:225], v238 offset:8192
	ds_read_b128 v[226:229], v238 offset:10240
	ds_read_b128 v[230:233], v238 offset:12288
	ds_read_b128 v[234:237], v238 offset:14336
	s_min_u32 s21, s20, 29
	s_xor_b32 s19, s19, 0x10000
	v_add_u32_e32 v239, s19, v189
	s_waitcnt vmcnt(11)
	v_cvt_pk_bf16_f32 v13, v12, v13
	v_cvt_pk_bf16_f32 v12, v10, v11
	s_waitcnt vmcnt(10)
	v_cvt_pk_bf16_f32 v11, v20, v21
	v_cvt_pk_bf16_f32 v10, v18, v19
	ds_write2st64_b64 v239, v[12:13], v[10:11] offset1:8
	s_waitcnt vmcnt(9)
	v_cvt_pk_bf16_f32 v11, v24, v25
	v_cvt_pk_bf16_f32 v10, v22, v23
	s_waitcnt vmcnt(8)
	v_cvt_pk_bf16_f32 v13, v32, v33
	v_cvt_pk_bf16_f32 v12, v30, v31
	ds_write2st64_b64 v239, v[10:11], v[12:13] offset0:16 offset1:24
	s_waitcnt vmcnt(7)
	v_cvt_pk_bf16_f32 v11, v36, v37
	v_cvt_pk_bf16_f32 v10, v34, v35
	s_waitcnt vmcnt(6)
	v_cvt_pk_bf16_f32 v13, v40, v41
	v_cvt_pk_bf16_f32 v12, v38, v39
	ds_write2st64_b64 v239, v[10:11], v[12:13] offset0:32 offset1:40
	s_waitcnt vmcnt(5)
	v_cvt_pk_bf16_f32 v11, v44, v45
	v_cvt_pk_bf16_f32 v10, v42, v43
	s_waitcnt vmcnt(4)
	v_cvt_pk_bf16_f32 v13, v48, v49
	v_cvt_pk_bf16_f32 v12, v46, v47
	ds_write2st64_b64 v239, v[10:11], v[12:13] offset0:48 offset1:56
	s_waitcnt lgkmcnt(0)
	s_add_i32 s21, s21, 2
	s_barrier
	s_setprio 1
	s_lshl_b32 s22, s21, 1
	s_and_b32 s22, s22, 0x60
	s_add_i32 s22, s22, s12
	s_lshl_b32 s22, s22, 6
	s_and_b32 s22, s22, 0x3f00
	s_or_b32 s22, s22, s13
	s_lshl_b32 s23, s21, 23
	s_lshl_b32 s22, s22, 9
	s_and_b32 s23, s23, 0x7000000
	s_or_b32 s22, s22, s23
	s_lshl_b32 s23, s21, 8
	s_and_b32 s23, s23, 0x100
	s_or_b32 s22, s22, s23
	s_or_b32 s23, s22, 0x4000
	s_waitcnt lgkmcnt(11)
	v_mfma_f32_16x16x32_bf16 v[174:177], v[178:181], v[206:209], v[174:177]
	v_mfma_f32_16x16x32_bf16 v[170:173], v[194:197], v[206:209], v[170:173]
	v_mfma_f32_16x16x32_bf16 v[158:161], v[198:201], v[206:209], v[158:161]
	buffer_load_dwordx4 v[10:13], v1, s[4:7], s22 offen sc0 nt
	v_mfma_f32_16x16x32_bf16 v[142:145], v[202:205], v[206:209], v[142:145]
	s_waitcnt lgkmcnt(10)
	v_mfma_f32_16x16x32_bf16 v[166:169], v[178:181], v[210:213], v[166:169]
	v_mfma_f32_16x16x32_bf16 v[162:165], v[194:197], v[210:213], v[162:165]
	v_mfma_f32_16x16x32_bf16 v[146:149], v[198:201], v[210:213], v[146:149]
	buffer_load_dwordx4 v[18:21], v1, s[4:7], s23 offen sc0 nt
	s_or_b32 s23, s22, 0x8000
	v_mfma_f32_16x16x32_bf16 v[122:125], v[202:205], v[210:213], v[122:125]
	s_waitcnt lgkmcnt(9)
	v_mfma_f32_16x16x32_bf16 v[154:157], v[178:181], v[214:217], v[154:157]
	v_mfma_f32_16x16x32_bf16 v[150:153], v[194:197], v[214:217], v[150:153]
	v_mfma_f32_16x16x32_bf16 v[130:133], v[198:201], v[214:217], v[130:133]
	buffer_load_dwordx4 v[22:25], v1, s[4:7], s23 offen sc0 nt
	s_or_b32 s23, s22, 0xc000
	v_mfma_f32_16x16x32_bf16 v[106:109], v[202:205], v[214:217], v[106:109]
	s_waitcnt lgkmcnt(8)
	v_mfma_f32_16x16x32_bf16 v[138:141], v[178:181], v[218:221], v[138:141]
	v_mfma_f32_16x16x32_bf16 v[134:137], v[194:197], v[218:221], v[134:137]
	v_mfma_f32_16x16x32_bf16 v[114:117], v[198:201], v[218:221], v[114:117]
	buffer_load_dwordx4 v[30:33], v1, s[4:7], s23 offen sc0 nt
	s_or_b32 s23, s22, 0x10000
	v_mfma_f32_16x16x32_bf16 v[90:93], v[202:205], v[218:221], v[90:93]
	s_waitcnt lgkmcnt(7)
	v_mfma_f32_16x16x32_bf16 v[126:129], v[178:181], v[222:225], v[126:129]
	v_mfma_f32_16x16x32_bf16 v[118:121], v[194:197], v[222:225], v[118:121]
	v_mfma_f32_16x16x32_bf16 v[98:101], v[198:201], v[222:225], v[98:101]
	buffer_load_dwordx4 v[34:37], v1, s[4:7], s23 offen sc0 nt
	s_or_b32 s23, s22, 0x14000
	v_mfma_f32_16x16x32_bf16 v[74:77], v[202:205], v[222:225], v[74:77]
	s_waitcnt lgkmcnt(6)
	v_mfma_f32_16x16x32_bf16 v[110:113], v[178:181], v[226:229], v[110:113]
	v_mfma_f32_16x16x32_bf16 v[102:105], v[194:197], v[226:229], v[102:105]
	v_mfma_f32_16x16x32_bf16 v[82:85], v[198:201], v[226:229], v[82:85]
	buffer_load_dwordx4 v[38:41], v1, s[4:7], s23 offen sc0 nt
	s_or_b32 s23, s22, 0x18000
	s_or_b32 s22, s22, 0x1c000
	v_mfma_f32_16x16x32_bf16 v[62:65], v[202:205], v[226:229], v[62:65]
	s_waitcnt lgkmcnt(5)
	v_mfma_f32_16x16x32_bf16 v[94:97], v[178:181], v[230:233], v[94:97]
	v_mfma_f32_16x16x32_bf16 v[86:89], v[194:197], v[230:233], v[86:89]
	v_mfma_f32_16x16x32_bf16 v[70:73], v[198:201], v[230:233], v[70:73]
	buffer_load_dwordx4 v[42:45], v1, s[4:7], s23 offen sc0 nt
	v_mfma_f32_16x16x32_bf16 v[54:57], v[202:205], v[230:233], v[54:57]
	s_waitcnt lgkmcnt(4)
	v_mfma_f32_16x16x32_bf16 v[78:81], v[178:181], v[234:237], v[78:81]
	v_mfma_f32_16x16x32_bf16 v[66:69], v[194:197], v[234:237], v[66:69]
	v_mfma_f32_16x16x32_bf16 v[58:61], v[198:201], v[234:237], v[58:61]
	buffer_load_dwordx4 v[46:49], v1, s[4:7], s22 offen sc0 nt
	v_mfma_f32_16x16x32_bf16 v[50:53], v[202:205], v[234:237], v[50:53]
	s_setprio 0
	s_waitcnt lgkmcnt(0)
	s_barrier
	ds_read_b128 v[178:181], v182 offset:33792
	ds_read_b128 v[194:197], v182 offset:35840
	ds_read_b128 v[198:201], v182 offset:37888
	ds_read_b128 v[202:205], v182 offset:39936
	ds_read_b128 v[206:209], v238 offset:1024
	ds_read_b128 v[210:213], v238 offset:3072
	ds_read_b128 v[214:217], v238 offset:5120
	ds_read_b128 v[218:221], v238 offset:7168
	ds_read_b128 v[222:225], v238 offset:9216
	ds_read_b128 v[226:229], v238 offset:11264
	ds_read_b128 v[230:233], v238 offset:13312
	ds_read_b128 v[234:237], v238 offset:15360
	v_add_u32_e32 v182, s19, v190
	s_waitcnt vmcnt(11)
	ds_write_b128 v182, v[2:5] offset:32768
	s_waitcnt vmcnt(10)
	ds_write_b128 v182, v[6:9] offset:40960
	s_waitcnt vmcnt(9)
	ds_write_b128 v182, v[14:17] offset:49152
	s_waitcnt vmcnt(8)
	ds_write_b128 v182, v[26:29] offset:57344
	s_waitcnt lgkmcnt(0)
	s_barrier
	s_setprio 1
	s_lshl_b32 s21, s21, 7
	s_and_b32 s21, s21, 0x780
	s_or_b32 s21, s21, s14
	s_or_b32 s22, s21, 0x20000
	s_waitcnt lgkmcnt(11)
	v_mfma_f32_16x16x32_bf16 v[174:177], v[178:181], v[206:209], v[174:177]
	v_mfma_f32_16x16x32_bf16 v[170:173], v[194:197], v[206:209], v[170:173]
	v_mfma_f32_16x16x32_bf16 v[158:161], v[198:201], v[206:209], v[158:161]
	v_mfma_f32_16x16x32_bf16 v[142:145], v[202:205], v[206:209], v[142:145]
	s_waitcnt lgkmcnt(10)
	v_mfma_f32_16x16x32_bf16 v[166:169], v[178:181], v[210:213], v[166:169]
	v_mfma_f32_16x16x32_bf16 v[162:165], v[194:197], v[210:213], v[162:165]
	buffer_load_dwordx4 v[2:5], v188, s[0:3], s21 offen sc1
	v_mfma_f32_16x16x32_bf16 v[146:149], v[198:201], v[210:213], v[146:149]
	v_mfma_f32_16x16x32_bf16 v[122:125], v[202:205], v[210:213], v[122:125]
	s_waitcnt lgkmcnt(9)
	v_mfma_f32_16x16x32_bf16 v[154:157], v[178:181], v[214:217], v[154:157]
	v_mfma_f32_16x16x32_bf16 v[150:153], v[194:197], v[214:217], v[150:153]
	v_mfma_f32_16x16x32_bf16 v[130:133], v[198:201], v[214:217], v[130:133]
	v_mfma_f32_16x16x32_bf16 v[106:109], v[202:205], v[214:217], v[106:109]
	s_waitcnt lgkmcnt(8)
	v_mfma_f32_16x16x32_bf16 v[138:141], v[178:181], v[218:221], v[138:141]
	v_mfma_f32_16x16x32_bf16 v[134:137], v[194:197], v[218:221], v[134:137]
	buffer_load_dwordx4 v[6:9], v188, s[0:3], s22 offen sc1
	s_or_b32 s22, s21, 0x40000
	s_or_b32 s21, s21, 0x60000
	v_mfma_f32_16x16x32_bf16 v[114:117], v[198:201], v[218:221], v[114:117]
	v_mfma_f32_16x16x32_bf16 v[90:93], v[202:205], v[218:221], v[90:93]
	s_waitcnt lgkmcnt(7)
	v_mfma_f32_16x16x32_bf16 v[126:129], v[178:181], v[222:225], v[126:129]
	v_mfma_f32_16x16x32_bf16 v[118:121], v[194:197], v[222:225], v[118:121]
	v_mfma_f32_16x16x32_bf16 v[98:101], v[198:201], v[222:225], v[98:101]
	v_mfma_f32_16x16x32_bf16 v[74:77], v[202:205], v[222:225], v[74:77]
	s_waitcnt lgkmcnt(6)
	v_mfma_f32_16x16x32_bf16 v[110:113], v[178:181], v[226:229], v[110:113]
	v_mfma_f32_16x16x32_bf16 v[102:105], v[194:197], v[226:229], v[102:105]
	buffer_load_dwordx4 v[14:17], v188, s[0:3], s22 offen sc1
	v_mfma_f32_16x16x32_bf16 v[82:85], v[198:201], v[226:229], v[82:85]
	v_mfma_f32_16x16x32_bf16 v[62:65], v[202:205], v[226:229], v[62:65]
	s_waitcnt lgkmcnt(5)
	v_mfma_f32_16x16x32_bf16 v[94:97], v[178:181], v[230:233], v[94:97]
	v_mfma_f32_16x16x32_bf16 v[86:89], v[194:197], v[230:233], v[86:89]
	v_mfma_f32_16x16x32_bf16 v[70:73], v[198:201], v[230:233], v[70:73]
	v_mfma_f32_16x16x32_bf16 v[54:57], v[202:205], v[230:233], v[54:57]
	s_waitcnt lgkmcnt(4)
	v_mfma_f32_16x16x32_bf16 v[78:81], v[178:181], v[234:237], v[78:81]
	v_mfma_f32_16x16x32_bf16 v[66:69], v[194:197], v[234:237], v[66:69]
	buffer_load_dwordx4 v[26:29], v188, s[0:3], s21 offen sc1
	v_mfma_f32_16x16x32_bf16 v[58:61], v[198:201], v[234:237], v[58:61]
	v_mfma_f32_16x16x32_bf16 v[50:53], v[202:205], v[234:237], v[50:53]
	s_setprio 0
	s_and_b32 s21, s20, 15
	s_cmp_lg_u32 s21, 15
	s_cbranch_scc1 .LBB1_3
	s_cmp_eq_u32 s26, 0
	s_cbranch_scc1 .Lpd_g0
	s_and_b32 s21, s18, 32
	s_add_i32 s21, s21, s12
	s_lshl_b32 s21, s21, 6
	s_and_b32 s21, s21, 0x3f00
	v_add_lshl_u32 v182, v193, s21, 9
	v_lshl_add_u64 v[206:207], v[184:185], 0, v[182:183]
	v_add_co_u32_e32 v208, vcc, s8, v206
	s_nop 1
	v_addc_co_u32_e32 v209, vcc, 0, v207, vcc
	v_add_co_u32_e32 v210, vcc, s15, v206
	s_nop 1
	v_addc_co_u32_e32 v211, vcc, 0, v207, vcc
	v_add_co_u32_e32 v212, vcc, s9, v206
	s_nop 1
	v_addc_co_u32_e32 v213, vcc, 0, v207, vcc
	v_add_co_u32_e32 v214, vcc, s16, v206
	s_nop 1
	v_addc_co_u32_e32 v215, vcc, 0, v207, vcc
	v_add_co_u32_e32 v216, vcc, s10, v206
	s_nop 1
	v_addc_co_u32_e32 v217, vcc, 0, v207, vcc
	v_add_co_u32_e32 v218, vcc, s17, v206
	s_nop 1
	v_addc_co_u32_e32 v219, vcc, 0, v207, vcc
	v_add_co_u32_e32 v220, vcc, s11, v206
	s_nop 1
	v_addc_co_u32_e32 v221, vcc, 0, v207, vcc
	global_store_dwordx4 v[206:207], v[174:177], off
	global_store_dwordx4 v[206:207], v[170:173], off offset:64
	global_store_dwordx4 v[206:207], v[158:161], off offset:128
	global_store_dwordx4 v[206:207], v[142:145], off offset:192
	global_store_dwordx4 v[208:209], v[166:169], off
	global_store_dwordx4 v[208:209], v[162:165], off offset:64
	global_store_dwordx4 v[208:209], v[146:149], off offset:128
	global_store_dwordx4 v[208:209], v[122:125], off offset:192
	global_store_dwordx4 v[210:211], v[154:157], off
	global_store_dwordx4 v[210:211], v[150:153], off offset:64
	global_store_dwordx4 v[210:211], v[130:133], off offset:128
	global_store_dwordx4 v[210:211], v[106:109], off offset:192
	global_store_dwordx4 v[212:213], v[138:141], off
	global_store_dwordx4 v[212:213], v[134:137], off offset:64
	global_store_dwordx4 v[212:213], v[114:117], off offset:128
	global_store_dwordx4 v[212:213], v[90:93], off offset:192
	global_store_dwordx4 v[214:215], v[126:129], off
	global_store_dwordx4 v[214:215], v[118:121], off offset:64
	global_store_dwordx4 v[214:215], v[98:101], off offset:128
	global_store_dwordx4 v[214:215], v[74:77], off offset:192
	global_store_dwordx4 v[216:217], v[110:113], off
	global_store_dwordx4 v[216:217], v[102:105], off offset:64
	global_store_dwordx4 v[216:217], v[82:85], off offset:128
	global_store_dwordx4 v[216:217], v[62:65], off offset:192
	global_store_dwordx4 v[218:219], v[94:97], off
	global_store_dwordx4 v[218:219], v[86:89], off offset:64
	global_store_dwordx4 v[218:219], v[70:73], off offset:128
	global_store_dwordx4 v[218:219], v[54:57], off offset:192
	global_store_dwordx4 v[220:221], v[78:81], off
	global_store_dwordx4 v[220:221], v[66:69], off offset:64
	global_store_dwordx4 v[220:221], v[58:61], off offset:128
	global_store_dwordx4 v[220:221], v[50:53], off offset:192
	s_waitcnt lgkmcnt(0)
	s_barrier
	s_branch .Lpd_body
.Lpd_g0:
	s_waitcnt lgkmcnt(0)
	s_barrier
	s_and_b32 s21, s18, 32
	s_add_i32 s21, s21, s12
	s_lshl_b32 s21, s21, 6
	s_and_b32 s21, s21, 0x3f00
	v_add_lshl_u32 v182, v193, s21, 9
	v_lshl_add_u64 v[206:207], v[184:185], 0, v[182:183]
	v_add_co_u32_e32 v208, vcc, s8, v206
	s_nop 1
	v_addc_co_u32_e32 v209, vcc, 0, v207, vcc
	v_add_co_u32_e32 v210, vcc, s15, v206
	s_nop 1
	v_addc_co_u32_e32 v211, vcc, 0, v207, vcc
	v_add_co_u32_e32 v212, vcc, s9, v206
	s_nop 1
	v_addc_co_u32_e32 v213, vcc, 0, v207, vcc
	v_add_co_u32_e32 v214, vcc, s16, v206
	s_nop 1
	v_addc_co_u32_e32 v215, vcc, 0, v207, vcc
	v_add_co_u32_e32 v216, vcc, s10, v206
	s_nop 1
	v_addc_co_u32_e32 v217, vcc, 0, v207, vcc
	v_add_co_u32_e32 v218, vcc, s17, v206
	s_nop 1
	v_addc_co_u32_e32 v219, vcc, 0, v207, vcc
	v_add_co_u32_e32 v220, vcc, s11, v206
	s_nop 1
	v_addc_co_u32_e32 v221, vcc, 0, v207, vcc
	global_store_dwordx4 v[206:207], v[174:177], off
	global_store_dwordx4 v[206:207], v[170:173], off offset:64
	global_store_dwordx4 v[206:207], v[158:161], off offset:128
	global_store_dwordx4 v[206:207], v[142:145], off offset:192
	global_store_dwordx4 v[208:209], v[166:169], off
	global_store_dwordx4 v[208:209], v[162:165], off offset:64
	global_store_dwordx4 v[208:209], v[146:149], off offset:128
	global_store_dwordx4 v[208:209], v[122:125], off offset:192
	global_store_dwordx4 v[210:211], v[154:157], off
	global_store_dwordx4 v[210:211], v[150:153], off offset:64
	global_store_dwordx4 v[210:211], v[130:133], off offset:128
	global_store_dwordx4 v[210:211], v[106:109], off offset:192
	global_store_dwordx4 v[212:213], v[138:141], off
	global_store_dwordx4 v[212:213], v[134:137], off offset:64
	global_store_dwordx4 v[212:213], v[114:117], off offset:128
	global_store_dwordx4 v[212:213], v[90:93], off offset:192
	global_store_dwordx4 v[214:215], v[126:129], off
	global_store_dwordx4 v[214:215], v[118:121], off offset:64
	global_store_dwordx4 v[214:215], v[98:101], off offset:128
	global_store_dwordx4 v[214:215], v[74:77], off offset:192
	global_store_dwordx4 v[216:217], v[110:113], off
	global_store_dwordx4 v[216:217], v[102:105], off offset:64
	global_store_dwordx4 v[216:217], v[82:85], off offset:128
	global_store_dwordx4 v[216:217], v[62:65], off offset:192
	global_store_dwordx4 v[218:219], v[94:97], off
	global_store_dwordx4 v[218:219], v[86:89], off offset:64
	global_store_dwordx4 v[218:219], v[70:73], off offset:128
	global_store_dwordx4 v[218:219], v[54:57], off offset:192
	global_store_dwordx4 v[220:221], v[78:81], off
	global_store_dwordx4 v[220:221], v[66:69], off offset:64
	global_store_dwordx4 v[220:221], v[58:61], off offset:128
	global_store_dwordx4 v[220:221], v[50:53], off offset:192
.Lpd_body:
	s_add_i32 s20, s20, 1
	s_add_i32 s18, s18, 2
	v_add_u32_e32 v182, s19, v191
	v_add_u32_e32 v238, s19, v192
	ds_read_b128 v[178:181], v182 offset:32768
	ds_read_b128 v[194:197], v182 offset:34816
	ds_read_b128 v[198:201], v182 offset:36864
	ds_read_b128 v[202:205], v182 offset:38912
	ds_read_b128 v[206:209], v238
	ds_read_b128 v[210:213], v238 offset:2048
	ds_read_b128 v[214:217], v238 offset:4096
	ds_read_b128 v[218:221], v238 offset:6144
	ds_read_b128 v[222:225], v238 offset:8192
	ds_read_b128 v[226:229], v238 offset:10240
	ds_read_b128 v[230:233], v238 offset:12288
	ds_read_b128 v[234:237], v238 offset:14336
	s_min_u32 s21, s20, 29
	s_xor_b32 s19, s19, 0x10000
	v_add_u32_e32 v239, s19, v189
	s_waitcnt vmcnt(43)
	v_cvt_pk_bf16_f32 v13, v12, v13
	v_cvt_pk_bf16_f32 v12, v10, v11
	s_waitcnt vmcnt(42)
	v_cvt_pk_bf16_f32 v11, v20, v21
	v_cvt_pk_bf16_f32 v10, v18, v19
	ds_write2st64_b64 v239, v[12:13], v[10:11] offset1:8
	s_waitcnt vmcnt(41)
	v_cvt_pk_bf16_f32 v11, v24, v25
	v_cvt_pk_bf16_f32 v10, v22, v23
	s_waitcnt vmcnt(40)
	v_cvt_pk_bf16_f32 v13, v32, v33
	v_cvt_pk_bf16_f32 v12, v30, v31
	ds_write2st64_b64 v239, v[10:11], v[12:13] offset0:16 offset1:24
	s_waitcnt vmcnt(39)
	v_cvt_pk_bf16_f32 v11, v36, v37
	v_cvt_pk_bf16_f32 v10, v34, v35
	s_waitcnt vmcnt(38)
	v_cvt_pk_bf16_f32 v13, v40, v41
	v_cvt_pk_bf16_f32 v12, v38, v39
	ds_write2st64_b64 v239, v[10:11], v[12:13] offset0:32 offset1:40
	s_waitcnt vmcnt(37)
	v_cvt_pk_bf16_f32 v11, v44, v45
	v_cvt_pk_bf16_f32 v10, v42, v43
	s_waitcnt vmcnt(36)
	v_cvt_pk_bf16_f32 v13, v48, v49
	v_cvt_pk_bf16_f32 v12, v46, v47
	ds_write2st64_b64 v239, v[10:11], v[12:13] offset0:48 offset1:56
	s_waitcnt lgkmcnt(0)
	s_add_i32 s21, s21, 2
	s_barrier
	s_setprio 1
	s_lshl_b32 s22, s21, 1
	s_and_b32 s22, s22, 0x60
	s_add_i32 s22, s22, s12
	s_lshl_b32 s22, s22, 6
	s_and_b32 s22, s22, 0x3f00
	s_or_b32 s22, s22, s13
	s_lshl_b32 s23, s21, 23
	s_lshl_b32 s22, s22, 9
	s_and_b32 s23, s23, 0x7000000
	s_or_b32 s22, s22, s23
	s_lshl_b32 s23, s21, 8
	s_and_b32 s23, s23, 0x100
	s_or_b32 s22, s22, s23
	s_or_b32 s23, s22, 0x4000
	s_waitcnt lgkmcnt(11)
	v_mfma_f32_16x16x32_bf16 v[174:177], v[178:181], v[206:209], v[240:243]
	v_mfma_f32_16x16x32_bf16 v[170:173], v[194:197], v[206:209], v[244:247]
	v_mfma_f32_16x16x32_bf16 v[158:161], v[198:201], v[206:209], v[248:251]
	buffer_load_dwordx4 v[10:13], v1, s[4:7], s22 offen sc0 nt
	v_mfma_f32_16x16x32_bf16 v[142:145], v[202:205], v[206:209], v[252:255]
	s_waitcnt lgkmcnt(10)
	v_mfma_f32_16x16x32_bf16 v[166:169], v[178:181], v[210:213], v[240:243]
	v_mfma_f32_16x16x32_bf16 v[162:165], v[194:197], v[210:213], v[244:247]
	v_mfma_f32_16x16x32_bf16 v[146:149], v[198:201], v[210:213], v[248:251]
	buffer_load_dwordx4 v[18:21], v1, s[4:7], s23 offen sc0 nt
	s_or_b32 s23, s22, 0x8000
	v_mfma_f32_16x16x32_bf16 v[122:125], v[202:205], v[210:213], v[252:255]
	s_waitcnt lgkmcnt(9)
	v_mfma_f32_16x16x32_bf16 v[154:157], v[178:181], v[214:217], v[240:243]
	v_mfma_f32_16x16x32_bf16 v[150:153], v[194:197], v[214:217], v[244:247]
	v_mfma_f32_16x16x32_bf16 v[130:133], v[198:201], v[214:217], v[248:251]
	buffer_load_dwordx4 v[22:25], v1, s[4:7], s23 offen sc0 nt
	s_or_b32 s23, s22, 0xc000
	v_mfma_f32_16x16x32_bf16 v[106:109], v[202:205], v[214:217], v[252:255]
	s_waitcnt lgkmcnt(8)
	v_mfma_f32_16x16x32_bf16 v[138:141], v[178:181], v[218:221], v[240:243]
	v_mfma_f32_16x16x32_bf16 v[134:137], v[194:197], v[218:221], v[244:247]
	v_mfma_f32_16x16x32_bf16 v[114:117], v[198:201], v[218:221], v[248:251]
	buffer_load_dwordx4 v[30:33], v1, s[4:7], s23 offen sc0 nt
	s_or_b32 s23, s22, 0x10000
	v_mfma_f32_16x16x32_bf16 v[90:93], v[202:205], v[218:221], v[252:255]
	s_waitcnt lgkmcnt(7)
	v_mfma_f32_16x16x32_bf16 v[126:129], v[178:181], v[222:225], v[240:243]
	v_mfma_f32_16x16x32_bf16 v[118:121], v[194:197], v[222:225], v[244:247]
	v_mfma_f32_16x16x32_bf16 v[98:101], v[198:201], v[222:225], v[248:251]
	buffer_load_dwordx4 v[34:37], v1, s[4:7], s23 offen sc0 nt
	s_or_b32 s23, s22, 0x14000
	v_mfma_f32_16x16x32_bf16 v[74:77], v[202:205], v[222:225], v[252:255]
	s_waitcnt lgkmcnt(6)
	v_mfma_f32_16x16x32_bf16 v[110:113], v[178:181], v[226:229], v[240:243]
	v_mfma_f32_16x16x32_bf16 v[102:105], v[194:197], v[226:229], v[244:247]
	v_mfma_f32_16x16x32_bf16 v[82:85], v[198:201], v[226:229], v[248:251]
	buffer_load_dwordx4 v[38:41], v1, s[4:7], s23 offen sc0 nt
	s_or_b32 s23, s22, 0x18000
	s_or_b32 s22, s22, 0x1c000
	v_mfma_f32_16x16x32_bf16 v[62:65], v[202:205], v[226:229], v[252:255]
	s_waitcnt lgkmcnt(5)
	v_mfma_f32_16x16x32_bf16 v[94:97], v[178:181], v[230:233], v[240:243]
	v_mfma_f32_16x16x32_bf16 v[86:89], v[194:197], v[230:233], v[244:247]
	v_mfma_f32_16x16x32_bf16 v[70:73], v[198:201], v[230:233], v[248:251]
	buffer_load_dwordx4 v[42:45], v1, s[4:7], s23 offen sc0 nt
	v_mfma_f32_16x16x32_bf16 v[54:57], v[202:205], v[230:233], v[252:255]
	s_waitcnt lgkmcnt(4)
	v_mfma_f32_16x16x32_bf16 v[78:81], v[178:181], v[234:237], v[240:243]
	v_mfma_f32_16x16x32_bf16 v[66:69], v[194:197], v[234:237], v[244:247]
	v_mfma_f32_16x16x32_bf16 v[58:61], v[198:201], v[234:237], v[248:251]
	buffer_load_dwordx4 v[46:49], v1, s[4:7], s22 offen sc0 nt
	v_mfma_f32_16x16x32_bf16 v[50:53], v[202:205], v[234:237], v[252:255]
	s_setprio 0
	s_waitcnt lgkmcnt(0)
	s_barrier
	ds_read_b128 v[178:181], v182 offset:33792
	ds_read_b128 v[194:197], v182 offset:35840
	ds_read_b128 v[198:201], v182 offset:37888
	ds_read_b128 v[202:205], v182 offset:39936
	ds_read_b128 v[206:209], v238 offset:1024
	ds_read_b128 v[210:213], v238 offset:3072
	ds_read_b128 v[214:217], v238 offset:5120
	ds_read_b128 v[218:221], v238 offset:7168
	ds_read_b128 v[222:225], v238 offset:9216
	ds_read_b128 v[226:229], v238 offset:11264
	ds_read_b128 v[230:233], v238 offset:13312
	ds_read_b128 v[234:237], v238 offset:15360
	v_add_u32_e32 v182, s19, v190
	s_waitcnt vmcnt(43)
	ds_write_b128 v182, v[2:5] offset:32768
	s_waitcnt vmcnt(42)
	ds_write_b128 v182, v[6:9] offset:40960
	s_waitcnt vmcnt(41)
	ds_write_b128 v182, v[14:17] offset:49152
	s_waitcnt vmcnt(40)
	ds_write_b128 v182, v[26:29] offset:57344
	s_waitcnt lgkmcnt(0)
	s_barrier
	s_setprio 1
	s_lshl_b32 s21, s21, 7
	s_and_b32 s21, s21, 0x780
	s_or_b32 s21, s21, s14
	s_or_b32 s22, s21, 0x20000
	s_waitcnt lgkmcnt(11)
	v_mfma_f32_16x16x32_bf16 v[174:177], v[178:181], v[206:209], v[174:177]
	v_mfma_f32_16x16x32_bf16 v[170:173], v[194:197], v[206:209], v[170:173]
	v_mfma_f32_16x16x32_bf16 v[158:161], v[198:201], v[206:209], v[158:161]
	v_mfma_f32_16x16x32_bf16 v[142:145], v[202:205], v[206:209], v[142:145]
	s_waitcnt lgkmcnt(10)
	v_mfma_f32_16x16x32_bf16 v[166:169], v[178:181], v[210:213], v[166:169]
	v_mfma_f32_16x16x32_bf16 v[162:165], v[194:197], v[210:213], v[162:165]
	buffer_load_dwordx4 v[2:5], v188, s[0:3], s21 offen sc1
	v_mfma_f32_16x16x32_bf16 v[146:149], v[198:201], v[210:213], v[146:149]
	v_mfma_f32_16x16x32_bf16 v[122:125], v[202:205], v[210:213], v[122:125]
	s_waitcnt lgkmcnt(9)
	v_mfma_f32_16x16x32_bf16 v[154:157], v[178:181], v[214:217], v[154:157]
	v_mfma_f32_16x16x32_bf16 v[150:153], v[194:197], v[214:217], v[150:153]
	v_mfma_f32_16x16x32_bf16 v[130:133], v[198:201], v[214:217], v[130:133]
	v_mfma_f32_16x16x32_bf16 v[106:109], v[202:205], v[214:217], v[106:109]
	s_waitcnt lgkmcnt(8)
	v_mfma_f32_16x16x32_bf16 v[138:141], v[178:181], v[218:221], v[138:141]
	v_mfma_f32_16x16x32_bf16 v[134:137], v[194:197], v[218:221], v[134:137]
	buffer_load_dwordx4 v[6:9], v188, s[0:3], s22 offen sc1
	s_or_b32 s22, s21, 0x40000
	s_or_b32 s21, s21, 0x60000
	v_mfma_f32_16x16x32_bf16 v[114:117], v[198:201], v[218:221], v[114:117]
	v_mfma_f32_16x16x32_bf16 v[90:93], v[202:205], v[218:221], v[90:93]
	s_waitcnt lgkmcnt(7)
	v_mfma_f32_16x16x32_bf16 v[126:129], v[178:181], v[222:225], v[126:129]
	v_mfma_f32_16x16x32_bf16 v[118:121], v[194:197], v[222:225], v[118:121]
	v_mfma_f32_16x16x32_bf16 v[98:101], v[198:201], v[222:225], v[98:101]
	v_mfma_f32_16x16x32_bf16 v[74:77], v[202:205], v[222:225], v[74:77]
	s_waitcnt lgkmcnt(6)
	v_mfma_f32_16x16x32_bf16 v[110:113], v[178:181], v[226:229], v[110:113]
	v_mfma_f32_16x16x32_bf16 v[102:105], v[194:197], v[226:229], v[102:105]
	buffer_load_dwordx4 v[14:17], v188, s[0:3], s22 offen sc1
	v_mfma_f32_16x16x32_bf16 v[82:85], v[198:201], v[226:229], v[82:85]
	v_mfma_f32_16x16x32_bf16 v[62:65], v[202:205], v[226:229], v[62:65]
	s_waitcnt lgkmcnt(5)
	v_mfma_f32_16x16x32_bf16 v[94:97], v[178:181], v[230:233], v[94:97]
	v_mfma_f32_16x16x32_bf16 v[86:89], v[194:197], v[230:233], v[86:89]
	v_mfma_f32_16x16x32_bf16 v[70:73], v[198:201], v[230:233], v[70:73]
	v_mfma_f32_16x16x32_bf16 v[54:57], v[202:205], v[230:233], v[54:57]
	s_waitcnt lgkmcnt(4)
	v_mfma_f32_16x16x32_bf16 v[78:81], v[178:181], v[234:237], v[78:81]
	v_mfma_f32_16x16x32_bf16 v[66:69], v[194:197], v[234:237], v[66:69]
	buffer_load_dwordx4 v[26:29], v188, s[0:3], s21 offen sc1
	v_mfma_f32_16x16x32_bf16 v[58:61], v[198:201], v[234:237], v[58:61]
	v_mfma_f32_16x16x32_bf16 v[50:53], v[202:205], v[234:237], v[50:53]
	s_setprio 0
	s_branch .LBB1_3
.Lt30:
	v_add_u32_e32 v182, s19, v191
	v_add_u32_e32 v238, s19, v192
	ds_read_b128 v[178:181], v182 offset:32768
	ds_read_b128 v[194:197], v182 offset:34816
	ds_read_b128 v[198:201], v182 offset:36864
	ds_read_b128 v[202:205], v182 offset:38912
	ds_read_b128 v[206:209], v238
	ds_read_b128 v[210:213], v238 offset:2048
	ds_read_b128 v[214:217], v238 offset:4096
	ds_read_b128 v[218:221], v238 offset:6144
	ds_read_b128 v[222:225], v238 offset:8192
	ds_read_b128 v[226:229], v238 offset:10240
	ds_read_b128 v[230:233], v238 offset:12288
	ds_read_b128 v[234:237], v238 offset:14336
	s_min_u32 s21, s20, 29
	s_xor_b32 s19, s19, 0x10000
	v_add_u32_e32 v239, s19, v189
	s_waitcnt vmcnt(11)
	v_cvt_pk_bf16_f32 v13, v12, v13
	v_cvt_pk_bf16_f32 v12, v10, v11
	s_waitcnt vmcnt(10)
	v_cvt_pk_bf16_f32 v11, v20, v21
	v_cvt_pk_bf16_f32 v10, v18, v19
	ds_write2st64_b64 v239, v[12:13], v[10:11] offset1:8
	s_waitcnt vmcnt(9)
	v_cvt_pk_bf16_f32 v11, v24, v25
	v_cvt_pk_bf16_f32 v10, v22, v23
	s_waitcnt vmcnt(8)
	v_cvt_pk_bf16_f32 v13, v32, v33
	v_cvt_pk_bf16_f32 v12, v30, v31
	ds_write2st64_b64 v239, v[10:11], v[12:13] offset0:16 offset1:24
	s_waitcnt vmcnt(7)
	v_cvt_pk_bf16_f32 v11, v36, v37
	v_cvt_pk_bf16_f32 v10, v34, v35
	s_waitcnt vmcnt(6)
	v_cvt_pk_bf16_f32 v13, v40, v41
	v_cvt_pk_bf16_f32 v12, v38, v39
	ds_write2st64_b64 v239, v[10:11], v[12:13] offset0:32 offset1:40
	s_waitcnt vmcnt(5)
	v_cvt_pk_bf16_f32 v11, v44, v45
	v_cvt_pk_bf16_f32 v10, v42, v43
	s_waitcnt vmcnt(4)
	v_cvt_pk_bf16_f32 v13, v48, v49
	v_cvt_pk_bf16_f32 v12, v46, v47
	ds_write2st64_b64 v239, v[10:11], v[12:13] offset0:48 offset1:56
	s_waitcnt lgkmcnt(0)
	s_add_i32 s21, s21, 2
	s_barrier
	s_setprio 1
	s_lshl_b32 s22, s21, 1
	s_and_b32 s22, s22, 0x60
	s_add_i32 s22, s22, s12
	s_lshl_b32 s22, s22, 6
	s_and_b32 s22, s22, 0x3f00
	s_or_b32 s22, s22, s13
	s_lshl_b32 s23, s21, 23
	s_lshl_b32 s22, s22, 9
	s_and_b32 s23, s23, 0x7000000
	s_or_b32 s22, s22, s23
	s_lshl_b32 s23, s21, 8
	s_and_b32 s23, s23, 0x100
	s_or_b32 s22, s22, s23
	s_or_b32 s23, s22, 0x4000
	s_waitcnt lgkmcnt(11)
	v_mfma_f32_16x16x32_bf16 v[174:177], v[178:181], v[206:209], v[174:177]
	v_mfma_f32_16x16x32_bf16 v[170:173], v[194:197], v[206:209], v[170:173]
	v_mfma_f32_16x16x32_bf16 v[158:161], v[198:201], v[206:209], v[158:161]
	v_mfma_f32_16x16x32_bf16 v[142:145], v[202:205], v[206:209], v[142:145]
	s_waitcnt lgkmcnt(10)
	v_mfma_f32_16x16x32_bf16 v[166:169], v[178:181], v[210:213], v[166:169]
	v_mfma_f32_16x16x32_bf16 v[162:165], v[194:197], v[210:213], v[162:165]
	v_mfma_f32_16x16x32_bf16 v[146:149], v[198:201], v[210:213], v[146:149]
	s_or_b32 s23, s22, 0x8000
	v_mfma_f32_16x16x32_bf16 v[122:125], v[202:205], v[210:213], v[122:125]
	s_waitcnt lgkmcnt(9)
	v_mfma_f32_16x16x32_bf16 v[154:157], v[178:181], v[214:217], v[154:157]
	v_mfma_f32_16x16x32_bf16 v[150:153], v[194:197], v[214:217], v[150:153]
	v_mfma_f32_16x16x32_bf16 v[130:133], v[198:201], v[214:217], v[130:133]
	s_or_b32 s23, s22, 0xc000
	v_mfma_f32_16x16x32_bf16 v[106:109], v[202:205], v[214:217], v[106:109]
	s_waitcnt lgkmcnt(8)
	v_mfma_f32_16x16x32_bf16 v[138:141], v[178:181], v[218:221], v[138:141]
	v_mfma_f32_16x16x32_bf16 v[134:137], v[194:197], v[218:221], v[134:137]
	v_mfma_f32_16x16x32_bf16 v[114:117], v[198:201], v[218:221], v[114:117]
	s_or_b32 s23, s22, 0x10000
	v_mfma_f32_16x16x32_bf16 v[90:93], v[202:205], v[218:221], v[90:93]
	s_waitcnt lgkmcnt(7)
	v_mfma_f32_16x16x32_bf16 v[126:129], v[178:181], v[222:225], v[126:129]
	v_mfma_f32_16x16x32_bf16 v[118:121], v[194:197], v[222:225], v[118:121]
	v_mfma_f32_16x16x32_bf16 v[98:101], v[198:201], v[222:225], v[98:101]
	s_or_b32 s23, s22, 0x14000
	v_mfma_f32_16x16x32_bf16 v[74:77], v[202:205], v[222:225], v[74:77]
	s_waitcnt lgkmcnt(6)
	v_mfma_f32_16x16x32_bf16 v[110:113], v[178:181], v[226:229], v[110:113]
	v_mfma_f32_16x16x32_bf16 v[102:105], v[194:197], v[226:229], v[102:105]
	v_mfma_f32_16x16x32_bf16 v[82:85], v[198:201], v[226:229], v[82:85]
	s_or_b32 s23, s22, 0x18000
	s_or_b32 s22, s22, 0x1c000
	v_mfma_f32_16x16x32_bf16 v[62:65], v[202:205], v[226:229], v[62:65]
	s_waitcnt lgkmcnt(5)
	v_mfma_f32_16x16x32_bf16 v[94:97], v[178:181], v[230:233], v[94:97]
	v_mfma_f32_16x16x32_bf16 v[86:89], v[194:197], v[230:233], v[86:89]
	v_mfma_f32_16x16x32_bf16 v[70:73], v[198:201], v[230:233], v[70:73]
	v_mfma_f32_16x16x32_bf16 v[54:57], v[202:205], v[230:233], v[54:57]
	s_waitcnt lgkmcnt(4)
	v_mfma_f32_16x16x32_bf16 v[78:81], v[178:181], v[234:237], v[78:81]
	v_mfma_f32_16x16x32_bf16 v[66:69], v[194:197], v[234:237], v[66:69]
	v_mfma_f32_16x16x32_bf16 v[58:61], v[198:201], v[234:237], v[58:61]
	v_mfma_f32_16x16x32_bf16 v[50:53], v[202:205], v[234:237], v[50:53]
	s_setprio 0
	s_waitcnt lgkmcnt(0)
	s_barrier
	ds_read_b128 v[178:181], v182 offset:33792
	ds_read_b128 v[194:197], v182 offset:35840
	ds_read_b128 v[198:201], v182 offset:37888
	ds_read_b128 v[202:205], v182 offset:39936
	ds_read_b128 v[206:209], v238 offset:1024
	ds_read_b128 v[210:213], v238 offset:3072
	ds_read_b128 v[214:217], v238 offset:5120
	ds_read_b128 v[218:221], v238 offset:7168
	ds_read_b128 v[222:225], v238 offset:9216
	ds_read_b128 v[226:229], v238 offset:11264
	ds_read_b128 v[230:233], v238 offset:13312
	ds_read_b128 v[234:237], v238 offset:15360
	v_add_u32_e32 v182, s19, v190
	s_waitcnt vmcnt(3)
	ds_write_b128 v182, v[2:5] offset:32768
	s_waitcnt vmcnt(2)
	ds_write_b128 v182, v[6:9] offset:40960
	s_waitcnt vmcnt(1)
	ds_write_b128 v182, v[14:17] offset:49152
	s_waitcnt vmcnt(0)
	ds_write_b128 v182, v[26:29] offset:57344
	s_waitcnt lgkmcnt(0)
	s_barrier
	s_setprio 1
	s_lshl_b32 s21, s21, 7
	s_and_b32 s21, s21, 0x780
	s_or_b32 s21, s21, s14
	s_or_b32 s22, s21, 0x20000
	s_waitcnt lgkmcnt(11)
	v_mfma_f32_16x16x32_bf16 v[174:177], v[178:181], v[206:209], v[174:177]
	v_mfma_f32_16x16x32_bf16 v[170:173], v[194:197], v[206:209], v[170:173]
	v_mfma_f32_16x16x32_bf16 v[158:161], v[198:201], v[206:209], v[158:161]
	v_mfma_f32_16x16x32_bf16 v[142:145], v[202:205], v[206:209], v[142:145]
	s_waitcnt lgkmcnt(10)
	v_mfma_f32_16x16x32_bf16 v[166:169], v[178:181], v[210:213], v[166:169]
	v_mfma_f32_16x16x32_bf16 v[162:165], v[194:197], v[210:213], v[162:165]
	v_mfma_f32_16x16x32_bf16 v[146:149], v[198:201], v[210:213], v[146:149]
	v_mfma_f32_16x16x32_bf16 v[122:125], v[202:205], v[210:213], v[122:125]
	s_waitcnt lgkmcnt(9)
	v_mfma_f32_16x16x32_bf16 v[154:157], v[178:181], v[214:217], v[154:157]
	v_mfma_f32_16x16x32_bf16 v[150:153], v[194:197], v[214:217], v[150:153]
	v_mfma_f32_16x16x32_bf16 v[130:133], v[198:201], v[214:217], v[130:133]
	v_mfma_f32_16x16x32_bf16 v[106:109], v[202:205], v[214:217], v[106:109]
	s_waitcnt lgkmcnt(8)
	v_mfma_f32_16x16x32_bf16 v[138:141], v[178:181], v[218:221], v[138:141]
	v_mfma_f32_16x16x32_bf16 v[134:137], v[194:197], v[218:221], v[134:137]
	s_or_b32 s22, s21, 0x40000
	s_or_b32 s21, s21, 0x60000
	v_mfma_f32_16x16x32_bf16 v[114:117], v[198:201], v[218:221], v[114:117]
	v_mfma_f32_16x16x32_bf16 v[90:93], v[202:205], v[218:221], v[90:93]
	s_waitcnt lgkmcnt(7)
	v_mfma_f32_16x16x32_bf16 v[126:129], v[178:181], v[222:225], v[126:129]
	v_mfma_f32_16x16x32_bf16 v[118:121], v[194:197], v[222:225], v[118:121]
	v_mfma_f32_16x16x32_bf16 v[98:101], v[198:201], v[222:225], v[98:101]
	v_mfma_f32_16x16x32_bf16 v[74:77], v[202:205], v[222:225], v[74:77]
	s_waitcnt lgkmcnt(6)
	v_mfma_f32_16x16x32_bf16 v[110:113], v[178:181], v[226:229], v[110:113]
	v_mfma_f32_16x16x32_bf16 v[102:105], v[194:197], v[226:229], v[102:105]
	v_mfma_f32_16x16x32_bf16 v[82:85], v[198:201], v[226:229], v[82:85]
	v_mfma_f32_16x16x32_bf16 v[62:65], v[202:205], v[226:229], v[62:65]
	s_waitcnt lgkmcnt(5)
	v_mfma_f32_16x16x32_bf16 v[94:97], v[178:181], v[230:233], v[94:97]
	v_mfma_f32_16x16x32_bf16 v[86:89], v[194:197], v[230:233], v[86:89]
	v_mfma_f32_16x16x32_bf16 v[70:73], v[198:201], v[230:233], v[70:73]
	v_mfma_f32_16x16x32_bf16 v[54:57], v[202:205], v[230:233], v[54:57]
	s_waitcnt lgkmcnt(4)
	v_mfma_f32_16x16x32_bf16 v[78:81], v[178:181], v[234:237], v[78:81]
	v_mfma_f32_16x16x32_bf16 v[66:69], v[194:197], v[234:237], v[66:69]
	v_mfma_f32_16x16x32_bf16 v[58:61], v[198:201], v[234:237], v[58:61]
	v_mfma_f32_16x16x32_bf16 v[50:53], v[202:205], v[234:237], v[50:53]
	s_setprio 0
	s_waitcnt lgkmcnt(0)
	s_barrier
	s_add_i32 s20, s20, 1
	s_add_i32 s18, s18, 2
	v_add_u32_e32 v182, s19, v191
	v_add_u32_e32 v238, s19, v192
	ds_read_b128 v[178:181], v182 offset:32768
	ds_read_b128 v[194:197], v182 offset:34816
	ds_read_b128 v[198:201], v182 offset:36864
	ds_read_b128 v[202:205], v182 offset:38912
	ds_read_b128 v[206:209], v238
	ds_read_b128 v[210:213], v238 offset:2048
	ds_read_b128 v[214:217], v238 offset:4096
	ds_read_b128 v[218:221], v238 offset:6144
	ds_read_b128 v[222:225], v238 offset:8192
	ds_read_b128 v[226:229], v238 offset:10240
	ds_read_b128 v[230:233], v238 offset:12288
	ds_read_b128 v[234:237], v238 offset:14336
	s_min_u32 s21, s20, 29
	s_xor_b32 s19, s19, 0x10000
	v_add_u32_e32 v239, s19, v189
	s_waitcnt lgkmcnt(0)
	s_add_i32 s21, s21, 2
	s_barrier
	s_setprio 1
	s_lshl_b32 s22, s21, 1
	s_and_b32 s22, s22, 0x60
	s_add_i32 s22, s22, s12
	s_lshl_b32 s22, s22, 6
	s_and_b32 s22, s22, 0x3f00
	s_or_b32 s22, s22, s13
	s_lshl_b32 s23, s21, 23
	s_lshl_b32 s22, s22, 9
	s_and_b32 s23, s23, 0x7000000
	s_or_b32 s22, s22, s23
	s_lshl_b32 s23, s21, 8
	s_and_b32 s23, s23, 0x100
	s_or_b32 s22, s22, s23
	s_or_b32 s23, s22, 0x4000
	s_waitcnt lgkmcnt(11)
	v_mfma_f32_16x16x32_bf16 v[174:177], v[178:181], v[206:209], v[174:177]
	v_mfma_f32_16x16x32_bf16 v[170:173], v[194:197], v[206:209], v[170:173]
	v_mfma_f32_16x16x32_bf16 v[158:161], v[198:201], v[206:209], v[158:161]
	v_mfma_f32_16x16x32_bf16 v[142:145], v[202:205], v[206:209], v[142:145]
	s_waitcnt lgkmcnt(10)
	v_mfma_f32_16x16x32_bf16 v[166:169], v[178:181], v[210:213], v[166:169]
	v_mfma_f32_16x16x32_bf16 v[162:165], v[194:197], v[210:213], v[162:165]
	v_mfma_f32_16x16x32_bf16 v[146:149], v[198:201], v[210:213], v[146:149]
	s_or_b32 s23, s22, 0x8000
	v_mfma_f32_16x16x32_bf16 v[122:125], v[202:205], v[210:213], v[122:125]
	s_waitcnt lgkmcnt(9)
	v_mfma_f32_16x16x32_bf16 v[154:157], v[178:181], v[214:217], v[154:157]
	v_mfma_f32_16x16x32_bf16 v[150:153], v[194:197], v[214:217], v[150:153]
	v_mfma_f32_16x16x32_bf16 v[130:133], v[198:201], v[214:217], v[130:133]
	s_or_b32 s23, s22, 0xc000
	v_mfma_f32_16x16x32_bf16 v[106:109], v[202:205], v[214:217], v[106:109]
	s_waitcnt lgkmcnt(8)
	v_mfma_f32_16x16x32_bf16 v[138:141], v[178:181], v[218:221], v[138:141]
	v_mfma_f32_16x16x32_bf16 v[134:137], v[194:197], v[218:221], v[134:137]
	v_mfma_f32_16x16x32_bf16 v[114:117], v[198:201], v[218:221], v[114:117]
	s_or_b32 s23, s22, 0x10000
	v_mfma_f32_16x16x32_bf16 v[90:93], v[202:205], v[218:221], v[90:93]
	s_waitcnt lgkmcnt(7)
	v_mfma_f32_16x16x32_bf16 v[126:129], v[178:181], v[222:225], v[126:129]
	v_mfma_f32_16x16x32_bf16 v[118:121], v[194:197], v[222:225], v[118:121]
	v_mfma_f32_16x16x32_bf16 v[98:101], v[198:201], v[222:225], v[98:101]
	s_or_b32 s23, s22, 0x14000
	v_mfma_f32_16x16x32_bf16 v[74:77], v[202:205], v[222:225], v[74:77]
	s_waitcnt lgkmcnt(6)
	v_mfma_f32_16x16x32_bf16 v[110:113], v[178:181], v[226:229], v[110:113]
	v_mfma_f32_16x16x32_bf16 v[102:105], v[194:197], v[226:229], v[102:105]
	v_mfma_f32_16x16x32_bf16 v[82:85], v[198:201], v[226:229], v[82:85]
	s_or_b32 s23, s22, 0x18000
	s_or_b32 s22, s22, 0x1c000
	v_mfma_f32_16x16x32_bf16 v[62:65], v[202:205], v[226:229], v[62:65]
	s_waitcnt lgkmcnt(5)
	v_mfma_f32_16x16x32_bf16 v[94:97], v[178:181], v[230:233], v[94:97]
	v_mfma_f32_16x16x32_bf16 v[86:89], v[194:197], v[230:233], v[86:89]
	v_mfma_f32_16x16x32_bf16 v[70:73], v[198:201], v[230:233], v[70:73]
	v_mfma_f32_16x16x32_bf16 v[54:57], v[202:205], v[230:233], v[54:57]
	s_waitcnt lgkmcnt(4)
	v_mfma_f32_16x16x32_bf16 v[78:81], v[178:181], v[234:237], v[78:81]
	v_mfma_f32_16x16x32_bf16 v[66:69], v[194:197], v[234:237], v[66:69]
	v_mfma_f32_16x16x32_bf16 v[58:61], v[198:201], v[234:237], v[58:61]
	v_mfma_f32_16x16x32_bf16 v[50:53], v[202:205], v[234:237], v[50:53]
	s_setprio 0
	s_waitcnt lgkmcnt(0)
	s_barrier
	ds_read_b128 v[178:181], v182 offset:33792
	ds_read_b128 v[194:197], v182 offset:35840
	ds_read_b128 v[198:201], v182 offset:37888
	ds_read_b128 v[202:205], v182 offset:39936
	ds_read_b128 v[206:209], v238 offset:1024
	ds_read_b128 v[210:213], v238 offset:3072
	ds_read_b128 v[214:217], v238 offset:5120
	ds_read_b128 v[218:221], v238 offset:7168
	ds_read_b128 v[222:225], v238 offset:9216
	ds_read_b128 v[226:229], v238 offset:11264
	ds_read_b128 v[230:233], v238 offset:13312
	ds_read_b128 v[234:237], v238 offset:15360
	s_waitcnt lgkmcnt(0)
	s_barrier
	s_setprio 1
	s_lshl_b32 s21, s21, 7
	s_and_b32 s21, s21, 0x780
	s_or_b32 s21, s21, s14
	s_or_b32 s22, s21, 0x20000
	s_waitcnt lgkmcnt(11)
	v_mfma_f32_16x16x32_bf16 v[174:177], v[178:181], v[206:209], v[174:177]
	v_mfma_f32_16x16x32_bf16 v[170:173], v[194:197], v[206:209], v[170:173]
	v_mfma_f32_16x16x32_bf16 v[158:161], v[198:201], v[206:209], v[158:161]
	v_mfma_f32_16x16x32_bf16 v[142:145], v[202:205], v[206:209], v[142:145]
	s_waitcnt lgkmcnt(10)
	v_mfma_f32_16x16x32_bf16 v[166:169], v[178:181], v[210:213], v[166:169]
	v_mfma_f32_16x16x32_bf16 v[162:165], v[194:197], v[210:213], v[162:165]
	v_mfma_f32_16x16x32_bf16 v[146:149], v[198:201], v[210:213], v[146:149]
	v_mfma_f32_16x16x32_bf16 v[122:125], v[202:205], v[210:213], v[122:125]
	s_waitcnt lgkmcnt(9)
	v_mfma_f32_16x16x32_bf16 v[154:157], v[178:181], v[214:217], v[154:157]
	v_mfma_f32_16x16x32_bf16 v[150:153], v[194:197], v[214:217], v[150:153]
	v_mfma_f32_16x16x32_bf16 v[130:133], v[198:201], v[214:217], v[130:133]
	v_mfma_f32_16x16x32_bf16 v[106:109], v[202:205], v[214:217], v[106:109]
	s_waitcnt lgkmcnt(8)
	v_mfma_f32_16x16x32_bf16 v[138:141], v[178:181], v[218:221], v[138:141]
	v_mfma_f32_16x16x32_bf16 v[134:137], v[194:197], v[218:221], v[134:137]
	s_or_b32 s22, s21, 0x40000
	s_or_b32 s21, s21, 0x60000
	v_mfma_f32_16x16x32_bf16 v[114:117], v[198:201], v[218:221], v[114:117]
	v_mfma_f32_16x16x32_bf16 v[90:93], v[202:205], v[218:221], v[90:93]
	s_waitcnt lgkmcnt(7)
	v_mfma_f32_16x16x32_bf16 v[126:129], v[178:181], v[222:225], v[126:129]
	v_mfma_f32_16x16x32_bf16 v[118:121], v[194:197], v[222:225], v[118:121]
	v_mfma_f32_16x16x32_bf16 v[98:101], v[198:201], v[222:225], v[98:101]
	v_mfma_f32_16x16x32_bf16 v[74:77], v[202:205], v[222:225], v[74:77]
	s_waitcnt lgkmcnt(6)
	v_mfma_f32_16x16x32_bf16 v[110:113], v[178:181], v[226:229], v[110:113]
	v_mfma_f32_16x16x32_bf16 v[102:105], v[194:197], v[226:229], v[102:105]
	v_mfma_f32_16x16x32_bf16 v[82:85], v[198:201], v[226:229], v[82:85]
	v_mfma_f32_16x16x32_bf16 v[62:65], v[202:205], v[226:229], v[62:65]
	s_waitcnt lgkmcnt(5)
	v_mfma_f32_16x16x32_bf16 v[94:97], v[178:181], v[230:233], v[94:97]
	v_mfma_f32_16x16x32_bf16 v[86:89], v[194:197], v[230:233], v[86:89]
	v_mfma_f32_16x16x32_bf16 v[70:73], v[198:201], v[230:233], v[70:73]
	v_mfma_f32_16x16x32_bf16 v[54:57], v[202:205], v[230:233], v[54:57]
	s_waitcnt lgkmcnt(4)
	v_mfma_f32_16x16x32_bf16 v[78:81], v[178:181], v[234:237], v[78:81]
	v_mfma_f32_16x16x32_bf16 v[66:69], v[194:197], v[234:237], v[66:69]
	v_mfma_f32_16x16x32_bf16 v[58:61], v[198:201], v[234:237], v[58:61]
	v_mfma_f32_16x16x32_bf16 v[50:53], v[202:205], v[234:237], v[50:53]
	s_setprio 0
	s_waitcnt lgkmcnt(0)
	s_barrier
	s_cmp_lg_u32 s26, 0
	s_cbranch_scc1 .Lfin_st
	s_barrier
.Lfin_st:
	s_and_b32 s21, s18, 32
	s_add_i32 s21, s21, s12
	s_lshl_b32 s21, s21, 6
	s_and_b32 s21, s21, 0x3f00
	v_add_lshl_u32 v182, v193, s21, 9
	v_lshl_add_u64 v[206:207], v[184:185], 0, v[182:183]
	v_add_co_u32_e32 v208, vcc, s8, v206
	s_nop 1
	v_addc_co_u32_e32 v209, vcc, 0, v207, vcc
	v_add_co_u32_e32 v210, vcc, s15, v206
	s_nop 1
	v_addc_co_u32_e32 v211, vcc, 0, v207, vcc
	v_add_co_u32_e32 v212, vcc, s9, v206
	s_nop 1
	v_addc_co_u32_e32 v213, vcc, 0, v207, vcc
	v_add_co_u32_e32 v214, vcc, s16, v206
	s_nop 1
	v_addc_co_u32_e32 v215, vcc, 0, v207, vcc
	v_add_co_u32_e32 v216, vcc, s10, v206
	s_nop 1
	v_addc_co_u32_e32 v217, vcc, 0, v207, vcc
	v_add_co_u32_e32 v218, vcc, s17, v206
	s_nop 1
	v_addc_co_u32_e32 v219, vcc, 0, v207, vcc
	v_add_co_u32_e32 v220, vcc, s11, v206
	s_nop 1
	v_addc_co_u32_e32 v221, vcc, 0, v207, vcc
	global_store_dwordx4 v[206:207], v[174:177], off
	global_store_dwordx4 v[206:207], v[170:173], off offset:64
	global_store_dwordx4 v[206:207], v[158:161], off offset:128
	global_store_dwordx4 v[206:207], v[142:145], off offset:192
	global_store_dwordx4 v[208:209], v[166:169], off
	global_store_dwordx4 v[208:209], v[162:165], off offset:64
	global_store_dwordx4 v[208:209], v[146:149], off offset:128
	global_store_dwordx4 v[208:209], v[122:125], off offset:192
	global_store_dwordx4 v[210:211], v[154:157], off
	global_store_dwordx4 v[210:211], v[150:153], off offset:64
	global_store_dwordx4 v[210:211], v[130:133], off offset:128
	global_store_dwordx4 v[210:211], v[106:109], off offset:192
	global_store_dwordx4 v[212:213], v[138:141], off
	global_store_dwordx4 v[212:213], v[134:137], off offset:64
	global_store_dwordx4 v[212:213], v[114:117], off offset:128
	global_store_dwordx4 v[212:213], v[90:93], off offset:192
	global_store_dwordx4 v[214:215], v[126:129], off
	global_store_dwordx4 v[214:215], v[118:121], off offset:64
	global_store_dwordx4 v[214:215], v[98:101], off offset:128
	global_store_dwordx4 v[214:215], v[74:77], off offset:192
	global_store_dwordx4 v[216:217], v[110:113], off
	global_store_dwordx4 v[216:217], v[102:105], off offset:64
	global_store_dwordx4 v[216:217], v[82:85], off offset:128
	global_store_dwordx4 v[216:217], v[62:65], off offset:192
	global_store_dwordx4 v[218:219], v[94:97], off
	global_store_dwordx4 v[218:219], v[86:89], off offset:64
	global_store_dwordx4 v[218:219], v[70:73], off offset:128
	global_store_dwordx4 v[218:219], v[54:57], off offset:192
	global_store_dwordx4 v[220:221], v[78:81], off
	global_store_dwordx4 v[220:221], v[66:69], off offset:64
	global_store_dwordx4 v[220:221], v[58:61], off offset:128
	global_store_dwordx4 v[220:221], v[50:53], off offset:192
	s_endpgm
